# C2: software L2 prefetch of the next unit's gathered activation rows (K-tiles 2..7) at the start of the epilogue, 3 dword loads per thread
# speedup vs baseline: 1.0012x; 1.0000x over previous
; #define LAS __attribute__((address_space(3)))
; template <bool EMU> __device__ __forceinline__ float e2m3q(float y) { if constexpr (EMU) { y = fminf(fmaxf(y, -7.5f), 7.5f); return fabsf(y) < 1.f ? rintf(y * 8.f) * 0.125f : y; } else return y; }
;     __device__ __forceinline__ void operator()(const f32x4 (&acc)[2][2][4][2], const UnitD& u, int wr, int wc, int fr, int fq) const {
;         const int row0 = u.r0 + wr * 64 + fr, col0 = u.c0 + wc * 32 + 8 * fq;
;         const LAS float* bg = bl_lds + u.ui * 256 + wc * 32 + 8 * fq; const LAS float* bl = bg + 128;
;         f32x4 bgv[2], blv[2];
; #pragma unroll
;         for (int n = 0; n < 2; ++n) { bgv[n] = *(const LAS f32x4*)(bg + 4 * n); blv[n] = *(const LAS f32x4*)(bl + 4 * n); }
;         constexpr float SC = 1.f / (QS_X1 * QS_WUP);
; #pragma unroll
;         for (int ai = 0; ai < 2; ++ai)
; #pragma unroll
;             for (int m = 0; m < 4; ++m) { unsigned char* rowp = H + (size_t)(row0 + ai * 128 + m * 16) * DM + col0; u32x2 w;
; #pragma unroll
;                 for (int n = 0; n < 2; ++n) { const f32x4 g = acc[ai][0][m][n] * SC + bgv[n], l = acc[ai][1][m][n] * SC + blv[n];
;                     const f32x2 o0 = act2((f32x2){g[0], g[1]}, (f32x2){l[0], l[1]}), o1 = act2((f32x2){g[2], g[3]}, (f32x2){l[2], l[3]});
;                     int r = 0; r = __builtin_amdgcn_cvt_pk_fp8_f32(e2m3q<EMU_DOWN != 0>(o0.x), e2m3q<EMU_DOWN != 0>(o0.y), r, false); r = __builtin_amdgcn_cvt_pk_fp8_f32(e2m3q<EMU_DOWN != 0>(o1.x), e2m3q<EMU_DOWN != 0>(o1.y), r, true);
;                     if (n == 0) w.x = (unsigned)r; else w.y = (unsigned)r; }
.LBB0_755:
	s_add_u32 s18, s85, 0xffffff00
	v_mov_b32_e32 v16, v154
	v_bfe_u32 v152, v154, 4, 1
	s_addc_u32 s19, s86, -1
	s_lshl_b32 s20, s76, 10
	v_mul_u32_u24_e32 v152, 0x3ff8, v152
	v_lshrrev_b32_e32 v0, 1, v16
	v_and_b32_e32 v18, 0x60, v0
	v_and_b32_e32 v19, 24, v0
	s_add_i32 s20, s20, 0
	s_add_i32 s20, s20, 0x23100
	v_lshlrev_b32_e32 v0, 2, v18
	v_lshlrev_b32_e32 v1, 2, v19
	v_add3_u32 v4, s20, v0, v1
	s_lshl_b32 s20, s79, 10
	v_and_b32_e32 v216, 0xff, v154
	s_add_i32 s20, s20, 0x20000
	v_lshrrev_b32_e32 v217, 8, v154
	v_lshl_add_u32 v216, v216, 2, s20
	ds_read_b128 v[8:11], v4
	ds_read_b128 v[0:3], v4 offset:16
	ds_read_b128 v[12:15], v4 offset:512
	ds_read_b128 v[4:7], v4 offset:528
	ds_read_b32 v216, v216
	v_and_b32_e32 v17, 15, v16
	s_waitcnt lgkmcnt(0)
	v_mul_u32_u24_e32 v217, 0x180, v217
	s_nop 0
	v_lshl_add_u32 v216, v216, 10, v217
	global_load_dword v218, v216, s[0:1] offset:256
	global_load_dword v219, v216, s[0:1] offset:384
	global_load_dword v220, v216, s[0:1] offset:512
	v_pk_fma_f32 v[22:23], v[148:149], s[36:37], v[8:9] op_sel_hi:[1,0,1]
	v_ashrrev_i32_e32 v20, 2, v16
	v_min_f32_e32 v23, 0x40e00000, v23
	v_min_f32_e32 v22, 0x40e00000, v22
	v_pk_mul_f32 v[176:177], v[22:23], s[78:79] op_sel_hi:[1,0]
	v_pk_fma_f32 v[174:175], v[116:117], s[36:37], v[12:13] op_sel_hi:[1,0,1]
	v_exp_f32_e32 v176, v176
	v_exp_f32_e32 v177, v177
	v_and_or_b32 v17, v20, s39, v17
	v_pk_fma_f32 v[20:21], v[150:151], s[36:37], v[10:11] op_sel_hi:[1,0,1]
	v_med3_f32 v175, v175, s47, v190
	v_pk_add_f32 v[176:177], v[176:177], 1.0 op_sel_hi:[1,0]
	v_med3_f32 v174, v174, s47, v190
	v_rcp_f32_e32 v176, v176
	v_rcp_f32_e32 v177, v177
	v_pk_fma_f32 v[174:175], v[174:175], 4.0, 4.0 op_sel_hi:[1,0,0]
	v_min_f32_e32 v21, 0x40e00000, v21
	v_min_f32_e32 v20, 0x40e00000, v20
	v_pk_mul_f32 v[22:23], v[22:23], v[176:177]
	v_pk_fma_f32 v[172:173], v[118:119], s[36:37], v[14:15] op_sel_hi:[1,0,1]
	v_pk_mul_f32 v[22:23], v[174:175], v[22:23]
	v_pk_mul_f32 v[174:175], v[20:21], s[78:79] op_sel_hi:[1,0]
	v_med3_f32 v173, v173, s47, v190
	v_exp_f32_e32 v174, v174
	v_exp_f32_e32 v175, v175
	v_med3_f32 v172, v172, s47, v190
	v_pk_fma_f32 v[172:173], v[172:173], 4.0, 4.0 op_sel_hi:[1,0,0]
	v_pk_fma_f32 v[176:177], v[112:113], s[36:37], v[4:5] op_sel_hi:[1,0,1]
	v_pk_add_f32 v[174:175], v[174:175], 1.0 op_sel_hi:[1,0]
	v_med3_f32 v177, v177, s47, v190
	v_rcp_f32_e32 v174, v174
	v_rcp_f32_e32 v175, v175
	v_med3_f32 v176, v176, s47, v190
	v_pk_fma_f32 v[176:177], v[176:177], 4.0, 4.0 op_sel_hi:[1,0,0]
	v_add3_u32 v16, v18, s2, v19
	v_pk_mul_f32 v[20:21], v[20:21], v[174:175]
	v_pk_fma_f32 v[174:175], v[114:115], s[36:37], v[6:7] op_sel_hi:[1,0,1]
	v_pk_mul_f32 v[20:21], v[172:173], v[20:21]
	v_cvt_pk_fp8_f32 v148, v22, v23
	v_pk_fma_f32 v[22:23], v[144:145], s[36:37], v[0:1] op_sel_hi:[1,0,1]
	v_min_f32_e32 v23, 0x40e00000, v23
	v_min_f32_e32 v22, 0x40e00000, v22
	v_pk_mul_f32 v[178:179], v[22:23], s[78:79] op_sel_hi:[1,0]
	v_cvt_pk_fp8_f32 v148, v20, v21 op_sel:[0,0,1]
	v_exp_f32_e32 v178, v178
	v_exp_f32_e32 v179, v179
	v_pk_fma_f32 v[20:21], v[146:147], s[36:37], v[2:3] op_sel_hi:[1,0,1]
	v_med3_f32 v175, v175, s47, v190
	v_min_f32_e32 v21, 0x40e00000, v21
	v_pk_add_f32 v[178:179], v[178:179], 1.0 op_sel_hi:[1,0]
	v_min_f32_e32 v20, 0x40e00000, v20
	v_rcp_f32_e32 v178, v178
	v_rcp_f32_e32 v179, v179
	v_med3_f32 v174, v174, s47, v190
	v_pk_fma_f32 v[174:175], v[174:175], 4.0, 4.0 op_sel_hi:[1,0,0]
	v_add_u32_e32 v18, s68, v17
	v_pk_mul_f32 v[22:23], v[22:23], v[178:179]
	v_ashrrev_i32_e32 v19, 31, v18
	v_pk_mul_f32 v[22:23], v[176:177], v[22:23]
	v_pk_mul_f32 v[176:177], v[20:21], s[78:79] op_sel_hi:[1,0]
	v_cvt_pk_fp8_f32 v149, v22, v23
	v_exp_f32_e32 v176, v176
	v_exp_f32_e32 v177, v177
	v_lshlrev_b64 v[18:19], 10, v[18:19]
	v_ashrrev_i32_e32 v17, 31, v16
	v_lshl_add_u64 v[18:19], s[6:7], 0, v[18:19]
	v_pk_add_f32 v[176:177], v[176:177], 1.0 op_sel_hi:[1,0]
	v_lshl_add_u64 v[16:17], v[18:19], 0, v[16:17]
	s_nop 0
	v_lshl_add_u64 v[144:145], v[16:17], 0, v[152:153]
	v_rcp_f32_e32 v176, v176
	v_rcp_f32_e32 v177, v177
	v_pk_fma_f32 v[18:19], v[142:143], s[36:37], v[10:11] op_sel_hi:[1,0,1]
	v_pk_fma_f32 v[22:23], v[110:111], s[36:37], v[14:15] op_sel_hi:[1,0,1]
	v_min_f32_e32 v19, 0x40e00000, v19
	v_pk_mul_f32 v[20:21], v[20:21], v[176:177]
	v_min_f32_e32 v18, 0x40e00000, v18
	v_pk_mul_f32 v[20:21], v[174:175], v[20:21]
	v_med3_f32 v23, v23, s47, v190
	v_cvt_pk_fp8_f32 v149, v20, v21 op_sel:[0,0,1]
	v_pk_fma_f32 v[20:21], v[140:141], s[36:37], v[8:9] op_sel_hi:[1,0,1]
	v_med3_f32 v22, v22, s47, v190
	v_min_f32_e32 v21, 0x40e00000, v21
	v_min_f32_e32 v20, 0x40e00000, v20
	v_pk_mul_f32 v[174:175], v[20:21], s[78:79] op_sel_hi:[1,0]
	v_exp_f32_e32 v174, v174
	v_exp_f32_e32 v175, v175
	v_pk_fma_f32 v[172:173], v[108:109], s[36:37], v[12:13] op_sel_hi:[1,0,1]
	v_pk_fma_f32 v[22:23], v[22:23], 4.0, 4.0 op_sel_hi:[1,0,0]
	v_med3_f32 v173, v173, s47, v190
	v_pk_add_f32 v[174:175], v[174:175], 1.0 op_sel_hi:[1,0]
	v_med3_f32 v172, v172, s47, v190
	v_rcp_f32_e32 v174, v174
	v_rcp_f32_e32 v175, v175
	v_pk_fma_f32 v[172:173], v[172:173], 4.0, 4.0 op_sel_hi:[1,0,0]
	s_movk_i32 s20, 0x4000
	s_mov_b64 s[88:89], 0x42040080
	v_pk_mul_f32 v[20:21], v[20:21], v[174:175]
	v_pk_fma_f32 v[174:175], v[104:105], s[36:37], v[4:5] op_sel_hi:[1,0,1]
	v_pk_mul_f32 v[20:21], v[172:173], v[20:21]
	v_pk_mul_f32 v[172:173], v[18:19], s[78:79] op_sel_hi:[1,0]
	v_med3_f32 v175, v175, s47, v190
	v_exp_f32_e32 v172, v172
	v_exp_f32_e32 v173, v173
	v_med3_f32 v174, v174, s47, v190
	v_pk_fma_f32 v[174:175], v[174:175], 4.0, 4.0 op_sel_hi:[1,0,0]
	v_pk_add_f32 v[172:173], v[172:173], 1.0 op_sel_hi:[1,0]
; #define LAS __attribute__((address_space(3)))
; template <bool EMU> __device__ __forceinline__ float e2m3q(float y) { if constexpr (EMU) { y = fminf(fmaxf(y, -7.5f), 7.5f); return fabsf(y) < 1.f ? rintf(y * 8.f) * 0.125f : y; } else return y; }
;     static __device__ __forceinline__ f32x2 act2(f32x2 g, f32x2 l) {
;         g = __builtin_elementwise_min(g, (f32x2){7.f, 7.f}); l = __builtin_elementwise_min(__builtin_elementwise_max(l, (f32x2){-7.f, -7.f}), (f32x2){7.f, 7.f});
;         const f32x2 t = g * (-1.702f * 1.44269504089f); f32x2 e; e.x = __builtin_amdgcn_exp2f(t.x); e.y = __builtin_amdgcn_exp2f(t.y);
;         const f32x2 d = e + 1.0f; f32x2 r; r.x = __builtin_amdgcn_rcpf(d.x); r.y = __builtin_amdgcn_rcpf(d.y);
;         return (g * r) * (l * QS_ACT + QS_ACT);
;     }
;     __device__ __forceinline__ void operator()(const f32x4 (&acc)[2][2][4][2], const UnitD& u, int wr, int wc, int fr, int fq) const {
;         const int row0 = u.r0 + wr * 64 + fr, col0 = u.c0 + wc * 32 + 8 * fq;
;         const LAS float* bg = bl_lds + u.ui * 256 + wc * 32 + 8 * fq; const LAS float* bl = bg + 128;
;         f32x4 bgv[2], blv[2];
; #pragma unroll
;         for (int n = 0; n < 2; ++n) { bgv[n] = *(const LAS f32x4*)(bg + 4 * n); blv[n] = *(const LAS f32x4*)(bl + 4 * n); }
;         constexpr float SC = 1.f / (QS_X1 * QS_WUP);
; #pragma unroll
;         for (int ai = 0; ai < 2; ++ai)
; #pragma unroll
;             for (int m = 0; m < 4; ++m) { unsigned char* rowp = H + (size_t)(row0 + ai * 128 + m * 16) * DM + col0; u32x2 w;
; #pragma unroll
;                 for (int n = 0; n < 2; ++n) { const f32x4 g = acc[ai][0][m][n] * SC + bgv[n], l = acc[ai][1][m][n] * SC + blv[n];
;                     const f32x2 o0 = act2((f32x2){g[0], g[1]}, (f32x2){l[0], l[1]}), o1 = act2((f32x2){g[2], g[3]}, (f32x2){l[2], l[3]});
;                     int r = 0; r = __builtin_amdgcn_cvt_pk_fp8_f32(e2m3q<EMU_DOWN != 0>(o0.x), e2m3q<EMU_DOWN != 0>(o0.y), r, false); r = __builtin_amdgcn_cvt_pk_fp8_f32(e2m3q<EMU_DOWN != 0>(o1.x), e2m3q<EMU_DOWN != 0>(o1.y), r, true);
;                     if (n == 0) w.x = (unsigned)r; else w.y = (unsigned)r; }
	s_nop 0
	v_rcp_f32_e32 v172, v172
	v_rcp_f32_e32 v173, v173
	s_nop 0
	v_pk_mul_f32 v[18:19], v[18:19], v[172:173]
	s_nop 0
	v_pk_mul_f32 v[18:19], v[22:23], v[18:19]
	v_cvt_pk_fp8_f32 v150, v20, v21
	v_pk_fma_f32 v[20:21], v[136:137], s[36:37], v[0:1] op_sel_hi:[1,0,1]
	v_min_f32_e32 v21, 0x40e00000, v21
	v_min_f32_e32 v20, 0x40e00000, v20
	v_pk_mul_f32 v[176:177], v[20:21], s[78:79] op_sel_hi:[1,0]
	v_cvt_pk_fp8_f32 v150, v18, v19 op_sel:[0,0,1]
	v_exp_f32_e32 v176, v176
	v_exp_f32_e32 v177, v177
	v_pk_fma_f32 v[18:19], v[138:139], s[36:37], v[2:3] op_sel_hi:[1,0,1]
	v_pk_fma_f32 v[172:173], v[106:107], s[36:37], v[6:7] op_sel_hi:[1,0,1]
	v_min_f32_e32 v19, 0x40e00000, v19
	v_pk_add_f32 v[176:177], v[176:177], 1.0 op_sel_hi:[1,0]
	v_min_f32_e32 v18, 0x40e00000, v18
	v_rcp_f32_e32 v176, v176
	v_rcp_f32_e32 v177, v177
	v_med3_f32 v173, v173, s47, v190
	v_med3_f32 v172, v172, s47, v190
	v_pk_fma_f32 v[172:173], v[172:173], 4.0, 4.0 op_sel_hi:[1,0,0]
	v_pk_mul_f32 v[20:21], v[20:21], v[176:177]
	s_nop 0
	v_pk_mul_f32 v[20:21], v[174:175], v[20:21]
	v_pk_mul_f32 v[174:175], v[18:19], s[78:79] op_sel_hi:[1,0]
	v_cvt_pk_fp8_f32 v151, v20, v21
	v_exp_f32_e32 v174, v174
	v_exp_f32_e32 v175, v175
	v_pk_fma_f32 v[20:21], v[132:133], s[36:37], v[8:9] op_sel_hi:[1,0,1]
	v_pk_add_f32 v[174:175], v[174:175], 1.0 op_sel_hi:[1,0]
	s_nop 0
	v_rcp_f32_e32 v174, v174
	v_rcp_f32_e32 v175, v175
	v_min_f32_e32 v21, 0x40e00000, v21
	v_min_f32_e32 v20, 0x40e00000, v20
	v_pk_mul_f32 v[18:19], v[18:19], v[174:175]
	v_pk_mul_f32 v[174:175], v[20:21], s[78:79] op_sel_hi:[1,0]
	v_pk_mul_f32 v[18:19], v[172:173], v[18:19]
	v_exp_f32_e32 v174, v174
	v_exp_f32_e32 v175, v175
	v_cvt_pk_fp8_f32 v151, v18, v19 op_sel:[0,0,1]
	v_add_co_u32_e32 v18, vcc, s20, v16
	v_pk_add_f32 v[174:175], v[174:175], 1.0 op_sel_hi:[1,0]
	s_nop 0
	v_addc_co_u32_e32 v19, vcc, 0, v17, vcc
	v_rcp_f32_e32 v174, v174
	v_rcp_f32_e32 v175, v175
	v_pk_fma_f32 v[172:173], v[100:101], s[36:37], v[12:13] op_sel_hi:[1,0,1]
	v_permlane16_swap_b32_e32 v148, v150
	v_permlane16_swap_b32_e32 v149, v151
	global_store_dwordx4 v[144:145], v[148:151], off
	v_pk_fma_f32 v[18:19], v[134:135], s[36:37], v[10:11] op_sel_hi:[1,0,1]
	v_med3_f32 v173, v173, s47, v190
	v_med3_f32 v172, v172, s47, v190
	v_pk_mul_f32 v[20:21], v[20:21], v[174:175]
	v_pk_fma_f32 v[172:173], v[172:173], 4.0, 4.0 op_sel_hi:[1,0,0]
	v_min_f32_e32 v19, 0x40e00000, v19
	v_min_f32_e32 v18, 0x40e00000, v18
	v_pk_mul_f32 v[20:21], v[172:173], v[20:21]
	v_pk_mul_f32 v[172:173], v[18:19], s[78:79] op_sel_hi:[1,0]
	v_pk_fma_f32 v[22:23], v[102:103], s[36:37], v[14:15] op_sel_hi:[1,0,1]
	v_exp_f32_e32 v172, v172
	v_exp_f32_e32 v173, v173
	v_med3_f32 v23, v23, s47, v190
	v_med3_f32 v22, v22, s47, v190
	v_pk_fma_f32 v[22:23], v[22:23], 4.0, 4.0 op_sel_hi:[1,0,0]
	v_pk_add_f32 v[172:173], v[172:173], 1.0 op_sel_hi:[1,0]
	v_pk_fma_f32 v[174:175], v[96:97], s[36:37], v[4:5] op_sel_hi:[1,0,1]
	v_rcp_f32_e32 v172, v172
	v_rcp_f32_e32 v173, v173
	v_med3_f32 v175, v175, s47, v190
	v_med3_f32 v174, v174, s47, v190
	v_pk_fma_f32 v[174:175], v[174:175], 4.0, 4.0 op_sel_hi:[1,0,0]
	v_pk_mul_f32 v[18:19], v[18:19], v[172:173]
	v_pk_fma_f32 v[172:173], v[98:99], s[36:37], v[6:7] op_sel_hi:[1,0,1]
	v_pk_mul_f32 v[18:19], v[22:23], v[18:19]
	v_cvt_pk_fp8_f32 v148, v20, v21
	v_pk_fma_f32 v[20:21], v[128:129], s[36:37], v[0:1] op_sel_hi:[1,0,1]
	v_min_f32_e32 v21, 0x40e00000, v21
	v_min_f32_e32 v20, 0x40e00000, v20
	v_pk_mul_f32 v[176:177], v[20:21], s[78:79] op_sel_hi:[1,0]
	v_cvt_pk_fp8_f32 v148, v18, v19 op_sel:[0,0,1]
	v_exp_f32_e32 v176, v176
	v_exp_f32_e32 v177, v177
	v_pk_fma_f32 v[18:19], v[130:131], s[36:37], v[2:3] op_sel_hi:[1,0,1]
	v_med3_f32 v173, v173, s47, v190
	v_min_f32_e32 v19, 0x40e00000, v19
	v_pk_add_f32 v[176:177], v[176:177], 1.0 op_sel_hi:[1,0]
	v_min_f32_e32 v18, 0x40e00000, v18
	v_rcp_f32_e32 v176, v176
	v_rcp_f32_e32 v177, v177
	v_med3_f32 v172, v172, s47, v190
	v_pk_fma_f32 v[172:173], v[172:173], 4.0, 4.0 op_sel_hi:[1,0,0]
	s_mov_b32 s20, 0x8000
	v_pk_mul_f32 v[20:21], v[20:21], v[176:177]
	s_nop 0
	v_pk_mul_f32 v[20:21], v[174:175], v[20:21]
	v_pk_mul_f32 v[174:175], v[18:19], s[78:79] op_sel_hi:[1,0]
	v_cvt_pk_fp8_f32 v149, v20, v21
	v_exp_f32_e32 v174, v174
	v_exp_f32_e32 v175, v175
	v_pk_fma_f32 v[20:21], v[124:125], s[36:37], v[8:9] op_sel_hi:[1,0,1]
	v_pk_add_f32 v[174:175], v[174:175], 1.0 op_sel_hi:[1,0]
	s_nop 0
	v_rcp_f32_e32 v174, v174
	v_rcp_f32_e32 v175, v175
	v_min_f32_e32 v21, 0x40e00000, v21
	v_min_f32_e32 v20, 0x40e00000, v20
	v_pk_mul_f32 v[18:19], v[18:19], v[174:175]
	v_pk_mul_f32 v[174:175], v[20:21], s[78:79] op_sel_hi:[1,0]
	v_pk_mul_f32 v[18:19], v[172:173], v[18:19]
	v_exp_f32_e32 v174, v174
	v_exp_f32_e32 v175, v175
	v_cvt_pk_fp8_f32 v149, v18, v19 op_sel:[0,0,1]
	v_add_co_u32_e32 v18, vcc, s20, v16
	v_pk_add_f32 v[174:175], v[174:175], 1.0 op_sel_hi:[1,0]
	s_nop 0
	v_addc_co_u32_e32 v19, vcc, 0, v17, vcc
	v_rcp_f32_e32 v174, v174
	v_rcp_f32_e32 v175, v175
	v_pk_fma_f32 v[172:173], v[92:93], s[36:37], v[12:13] op_sel_hi:[1,0,1]
	v_lshl_add_u64 v[146:147], v[18:19], 0, v[152:153]
	v_pk_fma_f32 v[18:19], v[126:127], s[36:37], v[10:11] op_sel_hi:[1,0,1]
	v_med3_f32 v173, v173, s47, v190
	v_med3_f32 v172, v172, s47, v190
	v_pk_mul_f32 v[20:21], v[20:21], v[174:175]
	v_pk_fma_f32 v[172:173], v[172:173], 4.0, 4.0 op_sel_hi:[1,0,0]
	v_min_f32_e32 v19, 0x40e00000, v19
	v_min_f32_e32 v18, 0x40e00000, v18
	v_pk_mul_f32 v[20:21], v[172:173], v[20:21]
	v_pk_mul_f32 v[172:173], v[18:19], s[78:79] op_sel_hi:[1,0]
	v_pk_fma_f32 v[22:23], v[94:95], s[36:37], v[14:15] op_sel_hi:[1,0,1]
	v_exp_f32_e32 v172, v172
	v_exp_f32_e32 v173, v173
; #define LAS __attribute__((address_space(3)))
; template <bool EMU> __device__ __forceinline__ float e2m3q(float y) { if constexpr (EMU) { y = fminf(fmaxf(y, -7.5f), 7.5f); return fabsf(y) < 1.f ? rintf(y * 8.f) * 0.125f : y; } else return y; }
;     static __device__ __forceinline__ f32x2 act2(f32x2 g, f32x2 l) {
;         g = __builtin_elementwise_min(g, (f32x2){7.f, 7.f}); l = __builtin_elementwise_min(__builtin_elementwise_max(l, (f32x2){-7.f, -7.f}), (f32x2){7.f, 7.f});
;         const f32x2 t = g * (-1.702f * 1.44269504089f); f32x2 e; e.x = __builtin_amdgcn_exp2f(t.x); e.y = __builtin_amdgcn_exp2f(t.y);
;         const f32x2 d = e + 1.0f; f32x2 r; r.x = __builtin_amdgcn_rcpf(d.x); r.y = __builtin_amdgcn_rcpf(d.y);
;         return (g * r) * (l * QS_ACT + QS_ACT);
;     }
;     __device__ __forceinline__ void operator()(const f32x4 (&acc)[2][2][4][2], const UnitD& u, int wr, int wc, int fr, int fq) const {
;         const int row0 = u.r0 + wr * 64 + fr, col0 = u.c0 + wc * 32 + 8 * fq;
;         const LAS float* bg = bl_lds + u.ui * 256 + wc * 32 + 8 * fq; const LAS float* bl = bg + 128;
;         f32x4 bgv[2], blv[2];
; #pragma unroll
;         for (int n = 0; n < 2; ++n) { bgv[n] = *(const LAS f32x4*)(bg + 4 * n); blv[n] = *(const LAS f32x4*)(bl + 4 * n); }
;         constexpr float SC = 1.f / (QS_X1 * QS_WUP);
; #pragma unroll
;         for (int ai = 0; ai < 2; ++ai)
; #pragma unroll
;             for (int m = 0; m < 4; ++m) { unsigned char* rowp = H + (size_t)(row0 + ai * 128 + m * 16) * DM + col0; u32x2 w;
; #pragma unroll
;                 for (int n = 0; n < 2; ++n) { const f32x4 g = acc[ai][0][m][n] * SC + bgv[n], l = acc[ai][1][m][n] * SC + blv[n];
;                     const f32x2 o0 = act2((f32x2){g[0], g[1]}, (f32x2){l[0], l[1]}), o1 = act2((f32x2){g[2], g[3]}, (f32x2){l[2], l[3]});
;                     int r = 0; r = __builtin_amdgcn_cvt_pk_fp8_f32(e2m3q<EMU_DOWN != 0>(o0.x), e2m3q<EMU_DOWN != 0>(o0.y), r, false); r = __builtin_amdgcn_cvt_pk_fp8_f32(e2m3q<EMU_DOWN != 0>(o1.x), e2m3q<EMU_DOWN != 0>(o1.y), r, true);
;                     if (n == 0) w.x = (unsigned)r; else w.y = (unsigned)r; }
	v_med3_f32 v23, v23, s47, v190
	v_med3_f32 v22, v22, s47, v190
	v_pk_fma_f32 v[22:23], v[22:23], 4.0, 4.0 op_sel_hi:[1,0,0]
	v_pk_add_f32 v[172:173], v[172:173], 1.0 op_sel_hi:[1,0]
	v_pk_fma_f32 v[174:175], v[88:89], s[36:37], v[4:5] op_sel_hi:[1,0,1]
	v_rcp_f32_e32 v172, v172
	v_rcp_f32_e32 v173, v173
	v_med3_f32 v175, v175, s47, v190
	v_med3_f32 v174, v174, s47, v190
	v_pk_fma_f32 v[174:175], v[174:175], 4.0, 4.0 op_sel_hi:[1,0,0]
	v_pk_mul_f32 v[18:19], v[18:19], v[172:173]
	v_pk_fma_f32 v[172:173], v[90:91], s[36:37], v[6:7] op_sel_hi:[1,0,1]
	v_pk_mul_f32 v[18:19], v[22:23], v[18:19]
	v_cvt_pk_fp8_f32 v150, v20, v21
	v_pk_fma_f32 v[20:21], v[120:121], s[36:37], v[0:1] op_sel_hi:[1,0,1]
	v_min_f32_e32 v21, 0x40e00000, v21
	v_min_f32_e32 v20, 0x40e00000, v20
	v_pk_mul_f32 v[176:177], v[20:21], s[78:79] op_sel_hi:[1,0]
	v_cvt_pk_fp8_f32 v150, v18, v19 op_sel:[0,0,1]
	v_exp_f32_e32 v176, v176
	v_exp_f32_e32 v177, v177
	v_pk_fma_f32 v[18:19], v[122:123], s[36:37], v[2:3] op_sel_hi:[1,0,1]
	v_med3_f32 v173, v173, s47, v190
	v_min_f32_e32 v19, 0x40e00000, v19
	v_pk_add_f32 v[176:177], v[176:177], 1.0 op_sel_hi:[1,0]
	v_min_f32_e32 v18, 0x40e00000, v18
	v_rcp_f32_e32 v176, v176
	v_rcp_f32_e32 v177, v177
	v_med3_f32 v172, v172, s47, v190
	v_pk_fma_f32 v[172:173], v[172:173], 4.0, 4.0 op_sel_hi:[1,0,0]
	s_mov_b32 s20, 0xc000
	v_pk_mul_f32 v[20:21], v[20:21], v[176:177]
	s_nop 0
	v_pk_mul_f32 v[20:21], v[174:175], v[20:21]
	v_pk_mul_f32 v[174:175], v[18:19], s[78:79] op_sel_hi:[1,0]
	v_cvt_pk_fp8_f32 v151, v20, v21
	v_exp_f32_e32 v174, v174
	v_exp_f32_e32 v175, v175
	v_pk_fma_f32 v[20:21], v[84:85], s[36:37], v[8:9] op_sel_hi:[1,0,1]
	v_pk_add_f32 v[174:175], v[174:175], 1.0 op_sel_hi:[1,0]
	s_nop 0
	v_rcp_f32_e32 v174, v174
	v_rcp_f32_e32 v175, v175
	v_min_f32_e32 v21, 0x40e00000, v21
	v_min_f32_e32 v20, 0x40e00000, v20
	v_pk_mul_f32 v[18:19], v[18:19], v[174:175]
	v_pk_mul_f32 v[174:175], v[20:21], s[78:79] op_sel_hi:[1,0]
	v_pk_mul_f32 v[18:19], v[172:173], v[18:19]
	v_exp_f32_e32 v174, v174
	v_exp_f32_e32 v175, v175
	v_cvt_pk_fp8_f32 v151, v18, v19 op_sel:[0,0,1]
	v_add_co_u32_e32 v18, vcc, s20, v16
	v_pk_add_f32 v[174:175], v[174:175], 1.0 op_sel_hi:[1,0]
	s_nop 0
	v_addc_co_u32_e32 v19, vcc, 0, v17, vcc
	v_rcp_f32_e32 v174, v174
	v_rcp_f32_e32 v175, v175
	v_pk_fma_f32 v[172:173], v[52:53], s[36:37], v[12:13] op_sel_hi:[1,0,1]
	v_permlane16_swap_b32_e32 v148, v150
	v_permlane16_swap_b32_e32 v149, v151
	global_store_dwordx4 v[146:147], v[148:151], off
	v_pk_fma_f32 v[18:19], v[86:87], s[36:37], v[10:11] op_sel_hi:[1,0,1]
	v_med3_f32 v173, v173, s47, v190
	v_med3_f32 v172, v172, s47, v190
	v_pk_mul_f32 v[20:21], v[20:21], v[174:175]
	v_pk_fma_f32 v[172:173], v[172:173], 4.0, 4.0 op_sel_hi:[1,0,0]
	v_min_f32_e32 v19, 0x40e00000, v19
	v_min_f32_e32 v18, 0x40e00000, v18
	v_pk_mul_f32 v[20:21], v[172:173], v[20:21]
	v_pk_mul_f32 v[172:173], v[18:19], s[78:79] op_sel_hi:[1,0]
	v_pk_fma_f32 v[22:23], v[54:55], s[36:37], v[14:15] op_sel_hi:[1,0,1]
	v_exp_f32_e32 v172, v172
	v_exp_f32_e32 v173, v173
	v_med3_f32 v23, v23, s47, v190
	v_med3_f32 v22, v22, s47, v190
	v_pk_fma_f32 v[22:23], v[22:23], 4.0, 4.0 op_sel_hi:[1,0,0]
	v_pk_add_f32 v[172:173], v[172:173], 1.0 op_sel_hi:[1,0]
	v_pk_fma_f32 v[174:175], v[48:49], s[36:37], v[4:5] op_sel_hi:[1,0,1]
	v_rcp_f32_e32 v172, v172
	v_rcp_f32_e32 v173, v173
	v_med3_f32 v175, v175, s47, v190
	v_med3_f32 v174, v174, s47, v190
	v_pk_fma_f32 v[174:175], v[174:175], 4.0, 4.0 op_sel_hi:[1,0,0]
	v_pk_mul_f32 v[18:19], v[18:19], v[172:173]
	v_pk_fma_f32 v[172:173], v[50:51], s[36:37], v[6:7] op_sel_hi:[1,0,1]
	v_pk_mul_f32 v[18:19], v[22:23], v[18:19]
	v_cvt_pk_fp8_f32 v148, v20, v21
	v_pk_fma_f32 v[20:21], v[80:81], s[36:37], v[0:1] op_sel_hi:[1,0,1]
	v_min_f32_e32 v21, 0x40e00000, v21
	v_min_f32_e32 v20, 0x40e00000, v20
	v_pk_mul_f32 v[176:177], v[20:21], s[78:79] op_sel_hi:[1,0]
	v_cvt_pk_fp8_f32 v148, v18, v19 op_sel:[0,0,1]
	v_exp_f32_e32 v176, v176
	v_exp_f32_e32 v177, v177
	v_pk_fma_f32 v[18:19], v[82:83], s[36:37], v[2:3] op_sel_hi:[1,0,1]
	v_med3_f32 v173, v173, s47, v190
	v_min_f32_e32 v19, 0x40e00000, v19
	v_pk_add_f32 v[176:177], v[176:177], 1.0 op_sel_hi:[1,0]
	v_min_f32_e32 v18, 0x40e00000, v18
	v_rcp_f32_e32 v176, v176
	v_rcp_f32_e32 v177, v177
	v_med3_f32 v172, v172, s47, v190
	v_pk_fma_f32 v[172:173], v[172:173], 4.0, 4.0 op_sel_hi:[1,0,0]
	s_mov_b32 s20, 0x20000
	v_pk_mul_f32 v[20:21], v[20:21], v[176:177]
	s_nop 0
	v_pk_mul_f32 v[20:21], v[174:175], v[20:21]
	v_pk_mul_f32 v[174:175], v[18:19], s[78:79] op_sel_hi:[1,0]
	v_cvt_pk_fp8_f32 v149, v20, v21
	v_exp_f32_e32 v174, v174
	v_exp_f32_e32 v175, v175
	v_pk_fma_f32 v[20:21], v[76:77], s[36:37], v[8:9] op_sel_hi:[1,0,1]
	v_pk_add_f32 v[174:175], v[174:175], 1.0 op_sel_hi:[1,0]
	s_nop 0
	v_rcp_f32_e32 v174, v174
	v_rcp_f32_e32 v175, v175
	v_min_f32_e32 v21, 0x40e00000, v21
	v_min_f32_e32 v20, 0x40e00000, v20
	v_pk_mul_f32 v[18:19], v[18:19], v[174:175]
	v_pk_mul_f32 v[174:175], v[20:21], s[78:79] op_sel_hi:[1,0]
	v_pk_mul_f32 v[18:19], v[172:173], v[18:19]
	v_exp_f32_e32 v174, v174
	v_exp_f32_e32 v175, v175
	v_cvt_pk_fp8_f32 v149, v18, v19 op_sel:[0,0,1]
	v_add_co_u32_e32 v18, vcc, s20, v16
	v_pk_add_f32 v[174:175], v[174:175], 1.0 op_sel_hi:[1,0]
	s_nop 0
	v_addc_co_u32_e32 v19, vcc, 0, v17, vcc
	v_rcp_f32_e32 v174, v174
	v_rcp_f32_e32 v175, v175
	v_pk_fma_f32 v[172:173], v[44:45], s[36:37], v[12:13] op_sel_hi:[1,0,1]
	v_lshl_add_u64 v[146:147], v[18:19], 0, v[152:153]
	v_pk_fma_f32 v[18:19], v[78:79], s[36:37], v[10:11] op_sel_hi:[1,0,1]
	v_med3_f32 v173, v173, s47, v190
	v_med3_f32 v172, v172, s47, v190
	v_pk_mul_f32 v[20:21], v[20:21], v[174:175]
; #define LAS __attribute__((address_space(3)))
; template <bool EMU> __device__ __forceinline__ float e2m3q(float y) { if constexpr (EMU) { y = fminf(fmaxf(y, -7.5f), 7.5f); return fabsf(y) < 1.f ? rintf(y * 8.f) * 0.125f : y; } else return y; }
;     static __device__ __forceinline__ f32x2 act2(f32x2 g, f32x2 l) {
;         g = __builtin_elementwise_min(g, (f32x2){7.f, 7.f}); l = __builtin_elementwise_min(__builtin_elementwise_max(l, (f32x2){-7.f, -7.f}), (f32x2){7.f, 7.f});
;         const f32x2 t = g * (-1.702f * 1.44269504089f); f32x2 e; e.x = __builtin_amdgcn_exp2f(t.x); e.y = __builtin_amdgcn_exp2f(t.y);
;         const f32x2 d = e + 1.0f; f32x2 r; r.x = __builtin_amdgcn_rcpf(d.x); r.y = __builtin_amdgcn_rcpf(d.y);
;         return (g * r) * (l * QS_ACT + QS_ACT);
;     }
;     __device__ __forceinline__ void operator()(const f32x4 (&acc)[2][2][4][2], const UnitD& u, int wr, int wc, int fr, int fq) const {
;         const int row0 = u.r0 + wr * 64 + fr, col0 = u.c0 + wc * 32 + 8 * fq;
;         const LAS float* bg = bl_lds + u.ui * 256 + wc * 32 + 8 * fq; const LAS float* bl = bg + 128;
;         f32x4 bgv[2], blv[2];
; #pragma unroll
;         for (int n = 0; n < 2; ++n) { bgv[n] = *(const LAS f32x4*)(bg + 4 * n); blv[n] = *(const LAS f32x4*)(bl + 4 * n); }
;         constexpr float SC = 1.f / (QS_X1 * QS_WUP);
; #pragma unroll
;         for (int ai = 0; ai < 2; ++ai)
; #pragma unroll
;             for (int m = 0; m < 4; ++m) { unsigned char* rowp = H + (size_t)(row0 + ai * 128 + m * 16) * DM + col0; u32x2 w;
; #pragma unroll
;                 for (int n = 0; n < 2; ++n) { const f32x4 g = acc[ai][0][m][n] * SC + bgv[n], l = acc[ai][1][m][n] * SC + blv[n];
;                     const f32x2 o0 = act2((f32x2){g[0], g[1]}, (f32x2){l[0], l[1]}), o1 = act2((f32x2){g[2], g[3]}, (f32x2){l[2], l[3]});
;                     int r = 0; r = __builtin_amdgcn_cvt_pk_fp8_f32(e2m3q<EMU_DOWN != 0>(o0.x), e2m3q<EMU_DOWN != 0>(o0.y), r, false); r = __builtin_amdgcn_cvt_pk_fp8_f32(e2m3q<EMU_DOWN != 0>(o1.x), e2m3q<EMU_DOWN != 0>(o1.y), r, true);
;                     if (n == 0) w.x = (unsigned)r; else w.y = (unsigned)r; }
	v_pk_fma_f32 v[172:173], v[172:173], 4.0, 4.0 op_sel_hi:[1,0,0]
	v_min_f32_e32 v19, 0x40e00000, v19
	v_min_f32_e32 v18, 0x40e00000, v18
	v_pk_mul_f32 v[20:21], v[172:173], v[20:21]
	v_pk_mul_f32 v[172:173], v[18:19], s[78:79] op_sel_hi:[1,0]
	v_pk_fma_f32 v[22:23], v[46:47], s[36:37], v[14:15] op_sel_hi:[1,0,1]
	v_exp_f32_e32 v172, v172
	v_exp_f32_e32 v173, v173
	v_med3_f32 v23, v23, s47, v190
	v_med3_f32 v22, v22, s47, v190
	v_pk_fma_f32 v[22:23], v[22:23], 4.0, 4.0 op_sel_hi:[1,0,0]
	v_pk_add_f32 v[172:173], v[172:173], 1.0 op_sel_hi:[1,0]
	v_pk_fma_f32 v[174:175], v[40:41], s[36:37], v[4:5] op_sel_hi:[1,0,1]
	v_rcp_f32_e32 v172, v172
	v_rcp_f32_e32 v173, v173
	v_med3_f32 v175, v175, s47, v190
	v_med3_f32 v174, v174, s47, v190
	v_pk_fma_f32 v[174:175], v[174:175], 4.0, 4.0 op_sel_hi:[1,0,0]
	v_pk_mul_f32 v[18:19], v[18:19], v[172:173]
	v_pk_fma_f32 v[172:173], v[42:43], s[36:37], v[6:7] op_sel_hi:[1,0,1]
	v_pk_mul_f32 v[18:19], v[22:23], v[18:19]
	v_cvt_pk_fp8_f32 v150, v20, v21
	v_pk_fma_f32 v[20:21], v[72:73], s[36:37], v[0:1] op_sel_hi:[1,0,1]
	v_min_f32_e32 v21, 0x40e00000, v21
	v_min_f32_e32 v20, 0x40e00000, v20
	v_pk_mul_f32 v[176:177], v[20:21], s[78:79] op_sel_hi:[1,0]
	v_cvt_pk_fp8_f32 v150, v18, v19 op_sel:[0,0,1]
	v_exp_f32_e32 v176, v176
	v_exp_f32_e32 v177, v177
	v_pk_fma_f32 v[18:19], v[74:75], s[36:37], v[2:3] op_sel_hi:[1,0,1]
	v_med3_f32 v173, v173, s47, v190
	v_min_f32_e32 v19, 0x40e00000, v19
	v_pk_add_f32 v[176:177], v[176:177], 1.0 op_sel_hi:[1,0]
	v_min_f32_e32 v18, 0x40e00000, v18
	v_rcp_f32_e32 v176, v176
	v_rcp_f32_e32 v177, v177
	v_med3_f32 v172, v172, s47, v190
	v_pk_fma_f32 v[172:173], v[172:173], 4.0, 4.0 op_sel_hi:[1,0,0]
	s_mov_b32 s20, 0x24000
	v_pk_mul_f32 v[20:21], v[20:21], v[176:177]
	s_nop 0
	v_pk_mul_f32 v[20:21], v[174:175], v[20:21]
	v_pk_mul_f32 v[174:175], v[18:19], s[78:79] op_sel_hi:[1,0]
	v_cvt_pk_fp8_f32 v151, v20, v21
	v_exp_f32_e32 v174, v174
	v_exp_f32_e32 v175, v175
	v_pk_fma_f32 v[20:21], v[68:69], s[36:37], v[8:9] op_sel_hi:[1,0,1]
	v_pk_fma_f32 v[8:9], v[60:61], s[36:37], v[8:9] op_sel_hi:[1,0,1]
	v_min_f32_e32 v21, 0x40e00000, v21
	v_pk_add_f32 v[174:175], v[174:175], 1.0 op_sel_hi:[1,0]
	v_min_f32_e32 v20, 0x40e00000, v20
	v_rcp_f32_e32 v174, v174
	v_rcp_f32_e32 v175, v175
	v_min_f32_e32 v9, 0x40e00000, v9
	v_min_f32_e32 v8, 0x40e00000, v8
	v_pk_mul_f32 v[18:19], v[18:19], v[174:175]
	v_pk_mul_f32 v[174:175], v[20:21], s[78:79] op_sel_hi:[1,0]
	v_pk_mul_f32 v[18:19], v[172:173], v[18:19]
	v_exp_f32_e32 v174, v174
	v_exp_f32_e32 v175, v175
	v_cvt_pk_fp8_f32 v151, v18, v19 op_sel:[0,0,1]
	v_add_co_u32_e32 v18, vcc, s20, v16
	v_pk_add_f32 v[174:175], v[174:175], 1.0 op_sel_hi:[1,0]
	s_nop 0
	v_addc_co_u32_e32 v19, vcc, 0, v17, vcc
	v_rcp_f32_e32 v174, v174
	v_rcp_f32_e32 v175, v175
	v_pk_fma_f32 v[172:173], v[36:37], s[36:37], v[12:13] op_sel_hi:[1,0,1]
	v_permlane16_swap_b32_e32 v148, v150
	v_permlane16_swap_b32_e32 v149, v151
	global_store_dwordx4 v[146:147], v[148:151], off
	v_pk_fma_f32 v[18:19], v[70:71], s[36:37], v[10:11] op_sel_hi:[1,0,1]
	v_med3_f32 v173, v173, s47, v190
	v_med3_f32 v172, v172, s47, v190
	v_pk_mul_f32 v[20:21], v[20:21], v[174:175]
	v_pk_fma_f32 v[172:173], v[172:173], 4.0, 4.0 op_sel_hi:[1,0,0]
	v_min_f32_e32 v19, 0x40e00000, v19
	v_min_f32_e32 v18, 0x40e00000, v18
	v_pk_mul_f32 v[20:21], v[172:173], v[20:21]
	v_pk_mul_f32 v[172:173], v[18:19], s[78:79] op_sel_hi:[1,0]
	v_pk_fma_f32 v[22:23], v[38:39], s[36:37], v[14:15] op_sel_hi:[1,0,1]
	v_exp_f32_e32 v172, v172
	v_exp_f32_e32 v173, v173
	v_med3_f32 v23, v23, s47, v190
	v_med3_f32 v22, v22, s47, v190
	v_pk_fma_f32 v[22:23], v[22:23], 4.0, 4.0 op_sel_hi:[1,0,0]
	v_pk_add_f32 v[172:173], v[172:173], 1.0 op_sel_hi:[1,0]
	v_pk_fma_f32 v[174:175], v[32:33], s[36:37], v[4:5] op_sel_hi:[1,0,1]
	v_rcp_f32_e32 v172, v172
	v_rcp_f32_e32 v173, v173
	v_med3_f32 v175, v175, s47, v190
	v_med3_f32 v174, v174, s47, v190
	v_pk_fma_f32 v[174:175], v[174:175], 4.0, 4.0 op_sel_hi:[1,0,0]
	v_pk_mul_f32 v[18:19], v[18:19], v[172:173]
	v_pk_fma_f32 v[172:173], v[34:35], s[36:37], v[6:7] op_sel_hi:[1,0,1]
	v_pk_mul_f32 v[18:19], v[22:23], v[18:19]
	v_cvt_pk_fp8_f32 v148, v20, v21
	v_pk_fma_f32 v[20:21], v[64:65], s[36:37], v[0:1] op_sel_hi:[1,0,1]
; template <int K, bool PERM, bool GATHER, int MODE  , class Sched, class Epi>
; __device__ __forceinline__ void gemm_phase(LAS unsigned char* lds, const Sched& S, const Epi& E, const LAS int* gtab, int wv) {
;     ...
;         if (!has_next) break;
; #pragma unroll
;         for (int a = 0; a < 2; ++a)
; #pragma unroll
;             for (int b = 0; b < 2; ++b)
; #pragma unroll
;                 for (int m = 0; m < 4; ++m)
; #pragma unroll
;     static __device__ __forceinline__ f32x2 act2(f32x2 g, f32x2 l) {
;         g = __builtin_elementwise_min(g, (f32x2){7.f, 7.f}); l = __builtin_elementwise_min(__builtin_elementwise_max(l, (f32x2){-7.f, -7.f}), (f32x2){7.f, 7.f});
;         const f32x2 t = g * (-1.702f * 1.44269504089f); f32x2 e; e.x = __builtin_amdgcn_exp2f(t.x); e.y = __builtin_amdgcn_exp2f(t.y);
;         const f32x2 d = e + 1.0f; f32x2 r; r.x = __builtin_amdgcn_rcpf(d.x); r.y = __builtin_amdgcn_rcpf(d.y);
;         return (g * r) * (l * QS_ACT + QS_ACT);
;     }
;     __device__ __forceinline__ void operator()(const f32x4 (&acc)[2][2][4][2], const UnitD& u, int wr, int wc, int fr, int fq) const {
;         const int row0 = u.r0 + wr * 64 + fr, col0 = u.c0 + wc * 32 + 8 * fq;
;         const LAS float* bg = bl_lds + u.ui * 256 + wc * 32 + 8 * fq; const LAS float* bl = bg + 128;
;         f32x4 bgv[2], blv[2];
; #pragma unroll
;         for (int n = 0; n < 2; ++n) { bgv[n] = *(const LAS f32x4*)(bg + 4 * n); blv[n] = *(const LAS f32x4*)(bl + 4 * n); }
;         constexpr float SC = 1.f / (QS_X1 * QS_WUP);
; #pragma unroll
;         for (int ai = 0; ai < 2; ++ai)
; #pragma unroll
;             for (int m = 0; m < 4; ++m) { unsigned char* rowp = H + (size_t)(row0 + ai * 128 + m * 16) * DM + col0; u32x2 w;
; #pragma unroll
;                 for (int n = 0; n < 2; ++n) { const f32x4 g = acc[ai][0][m][n] * SC + bgv[n], l = acc[ai][1][m][n] * SC + blv[n];
;                     const f32x2 o0 = act2((f32x2){g[0], g[1]}, (f32x2){l[0], l[1]}), o1 = act2((f32x2){g[2], g[3]}, (f32x2){l[2], l[3]});
;                     int r = 0; r = __builtin_amdgcn_cvt_pk_fp8_f32(e2m3q<EMU_DOWN != 0>(o0.x), e2m3q<EMU_DOWN != 0>(o0.y), r, false); r = __builtin_amdgcn_cvt_pk_fp8_f32(e2m3q<EMU_DOWN != 0>(o1.x), e2m3q<EMU_DOWN != 0>(o1.y), r, true);
;                     if (n == 0) w.x = (unsigned)r; else w.y = (unsigned)r; }
;                 *(u32x2*)rowp = w; }
	v_min_f32_e32 v21, 0x40e00000, v21
	v_min_f32_e32 v20, 0x40e00000, v20
	v_pk_mul_f32 v[176:177], v[20:21], s[78:79] op_sel_hi:[1,0]
	v_cvt_pk_fp8_f32 v148, v18, v19 op_sel:[0,0,1]
	v_exp_f32_e32 v176, v176
	v_exp_f32_e32 v177, v177
	v_pk_fma_f32 v[18:19], v[66:67], s[36:37], v[2:3] op_sel_hi:[1,0,1]
	v_med3_f32 v173, v173, s47, v190
	v_min_f32_e32 v19, 0x40e00000, v19
	v_pk_add_f32 v[176:177], v[176:177], 1.0 op_sel_hi:[1,0]
	v_min_f32_e32 v18, 0x40e00000, v18
	v_rcp_f32_e32 v176, v176
	v_rcp_f32_e32 v177, v177
	v_med3_f32 v172, v172, s47, v190
	v_pk_fma_f32 v[172:173], v[172:173], 4.0, 4.0 op_sel_hi:[1,0,0]
	s_mov_b32 s20, 0x28000
	v_pk_mul_f32 v[20:21], v[20:21], v[176:177]
	v_pk_fma_f32 v[12:13], v[28:29], s[36:37], v[12:13] op_sel_hi:[1,0,1]
	v_pk_mul_f32 v[20:21], v[174:175], v[20:21]
	v_pk_mul_f32 v[174:175], v[18:19], s[78:79] op_sel_hi:[1,0]
	v_cvt_pk_fp8_f32 v149, v20, v21
	v_exp_f32_e32 v174, v174
	v_exp_f32_e32 v175, v175
	v_pk_fma_f32 v[10:11], v[62:63], s[36:37], v[10:11] op_sel_hi:[1,0,1]
	v_med3_f32 v13, v13, s47, v190
	v_med3_f32 v12, v12, s47, v190
	v_pk_add_f32 v[174:175], v[174:175], 1.0 op_sel_hi:[1,0]
	v_pk_fma_f32 v[14:15], v[30:31], s[36:37], v[14:15] op_sel_hi:[1,0,1]
	v_rcp_f32_e32 v174, v174
	v_rcp_f32_e32 v175, v175
	v_pk_fma_f32 v[12:13], v[12:13], 4.0, 4.0 op_sel_hi:[1,0,0]
	v_min_f32_e32 v11, 0x40e00000, v11
	v_min_f32_e32 v10, 0x40e00000, v10
	v_pk_mul_f32 v[18:19], v[18:19], v[174:175]
	v_pk_fma_f32 v[0:1], v[56:57], s[36:37], v[0:1] op_sel_hi:[1,0,1]
	v_pk_mul_f32 v[18:19], v[172:173], v[18:19]
	v_min_f32_e32 v1, 0x40e00000, v1
	v_cvt_pk_fp8_f32 v149, v18, v19 op_sel:[0,0,1]
	v_add_co_u32_e32 v18, vcc, s20, v16
	v_min_f32_e32 v0, 0x40e00000, v0
	s_nop 0
	v_addc_co_u32_e32 v19, vcc, 0, v17, vcc
	v_lshl_add_u64 v[146:147], v[18:19], 0, v[152:153]
	v_pk_mul_f32 v[18:19], v[8:9], s[78:79] op_sel_hi:[1,0]
	v_pk_fma_f32 v[4:5], v[24:25], s[36:37], v[4:5] op_sel_hi:[1,0,1]
	v_exp_f32_e32 v18, v18
	v_exp_f32_e32 v19, v19
	v_pk_fma_f32 v[2:3], v[58:59], s[36:37], v[2:3] op_sel_hi:[1,0,1]
	v_med3_f32 v5, v5, s47, v190
	v_med3_f32 v4, v4, s47, v190
	v_pk_add_f32 v[18:19], v[18:19], 1.0 op_sel_hi:[1,0]
	v_pk_fma_f32 v[6:7], v[26:27], s[36:37], v[6:7] op_sel_hi:[1,0,1]
	v_rcp_f32_e32 v18, v18
	v_rcp_f32_e32 v19, v19
	v_pk_fma_f32 v[4:5], v[4:5], 4.0, 4.0 op_sel_hi:[1,0,0]
	v_min_f32_e32 v3, 0x40e00000, v3
	v_min_f32_e32 v2, 0x40e00000, v2
	v_pk_mul_f32 v[8:9], v[8:9], v[18:19]
	s_nop 0
	v_pk_mul_f32 v[8:9], v[12:13], v[8:9]
	v_med3_f32 v13, v15, s47, v190
	v_med3_f32 v12, v14, s47, v190
	v_pk_mul_f32 v[14:15], v[10:11], s[78:79] op_sel_hi:[1,0]
	v_pk_fma_f32 v[12:13], v[12:13], 4.0, 4.0 op_sel_hi:[1,0,0]
	v_exp_f32_e32 v14, v14
	v_exp_f32_e32 v15, v15
	s_nop 0
	v_pk_add_f32 v[14:15], v[14:15], 1.0 op_sel_hi:[1,0]
	s_nop 0
	v_rcp_f32_e32 v14, v14
	v_rcp_f32_e32 v15, v15
	s_nop 0
	v_pk_mul_f32 v[10:11], v[10:11], v[14:15]
	s_nop 0
	v_pk_mul_f32 v[10:11], v[12:13], v[10:11]
	v_cvt_pk_fp8_f32 v150, v8, v9
	v_pk_mul_f32 v[8:9], v[0:1], s[78:79] op_sel_hi:[1,0]
	v_exp_f32_e32 v8, v8
	v_exp_f32_e32 v9, v9
	v_cvt_pk_fp8_f32 v150, v10, v11 op_sel:[0,0,1]
	v_pk_add_f32 v[8:9], v[8:9], 1.0 op_sel_hi:[1,0]
	s_nop 0
	v_rcp_f32_e32 v8, v8
	v_rcp_f32_e32 v9, v9
	s_nop 0
	v_pk_mul_f32 v[0:1], v[0:1], v[8:9]
	s_nop 0
	v_pk_mul_f32 v[0:1], v[4:5], v[0:1]
	v_med3_f32 v5, v7, s47, v190
	v_med3_f32 v4, v6, s47, v190
	v_pk_mul_f32 v[6:7], v[2:3], s[78:79] op_sel_hi:[1,0]
	v_cvt_pk_fp8_f32 v151, v0, v1
	v_exp_f32_e32 v6, v6
	v_exp_f32_e32 v7, v7
	v_pk_fma_f32 v[4:5], v[4:5], 4.0, 4.0 op_sel_hi:[1,0,0]
	v_add_co_u32_e32 v0, vcc, 0x2c000, v16
	v_pk_add_f32 v[6:7], v[6:7], 1.0 op_sel_hi:[1,0]
	s_nop 0
	v_addc_co_u32_e32 v1, vcc, 0, v17, vcc
	v_rcp_f32_e32 v6, v6
	v_rcp_f32_e32 v7, v7
	s_andn2_b64 vcc, exec, s[16:17]
	v_pk_mul_f32 v[2:3], v[2:3], v[6:7]
	s_nop 0
	v_pk_mul_f32 v[2:3], v[4:5], v[2:3]
	s_nop 0
	v_cvt_pk_fp8_f32 v151, v2, v3 op_sel:[0,0,1]
	s_nop 1
	v_permlane16_swap_b32_e32 v148, v150
	v_permlane16_swap_b32_e32 v149, v151
	global_store_dwordx4 v[146:147], v[148:151], off
	s_cbranch_vccnz .LBB0_759
	s_andn2_b64 vcc, exec, s[4:5]
	s_mov_b32 s86, 0x2f9636c4
	s_cbranch_vccnz .LBB0_758
	s_barrier
